# top-k SLOT table transposed + the 16 per-thread slot words collected in registers and written with 4 dwordx4 stores (was 16 scattered dword stores)
# baseline (speedup 1.0000x reference)
; template <int VPT>
; __device__ __forceinline__ void topk_list(const Params& p, LAS unsigned char* lds, const float* a, int N, int cap, int rowbase, int mbase, int e) {
;     ...
;     if (active) {
; #pragma unroll
;         for (int j = 0; j < VPT; ++j) {
;             const int i = tid * VPT + j, row = rowbase + i; int slot = -1;
;             if (k[j] > T) slot = gtb++;
;             else if (k[j] == T) { if (eqb < need) slot = G + eqb; ++eqb; }
;             if (slot >= 0) { const int m = mbase + slot; WSP(int, OFF_RIDX)[e * MEXP + m] = row; WSP(float, OFF_GATE)[e * MEXP + m] = __uint_as_float(k[j] >> 2); WSP(int, OFF_SLOT)[row * 16 + e] = m; }
;             else WSP(int, OFF_SLOT)[row * 16 + e] = -1;
;         }
.LBB0_840:
	s_or_b64 exec, exec, s[4:5]
	v_mov_b32_e32 v216, v5
	s_and_saveexec_b64 s[4:5], s[70:71]
	s_xor_b64 s[4:5], exec, s[4:5]
	v_cmp_lt_i32_e64 s[24:25], v2, v11
	v_sub_u32_e32 v4, v2, v11
	v_add_u32_e32 v4, 0x400, v4
	v_cndmask_b32_e64 v5, 0, 1, s[64:65]
	s_and_b64 s[24:25], s[64:65], s[24:25]
	v_add_u32_e32 v2, v2, v5
	v_cndmask_b32_e64 v5, -1, v4, s[24:25]
	s_or_saveexec_b64 s[4:5], s[4:5]
	v_mov_b32_e32 v4, v3
	s_xor_b64 exec, exec, s[4:5]
	v_add_u32_e32 v4, 1, v3
	v_mov_b32_e32 v5, v3
	s_or_b64 exec, exec, s[4:5]
	v_add3_u32 v9, s68, v8, 1
	v_mov_b32_e32 v3, -1
	v_cmp_lt_i32_e64 s[24:25], -1, v5
	s_and_saveexec_b64 s[4:5], s[24:25]
	s_cbranch_execz .LBB0_846
	v_add_u32_e32 v3, s55, v5
	v_add_u32_e32 v38, s54, v3
	v_ashrrev_i32_e32 v39, 31, v38
	v_lshlrev_b64 v[38:39], 2, v[38:39]
	v_lshl_add_u64 v[40:41], s[84:85], 0, v[38:39]
	v_lshrrev_b32_e32 v5, 2, v36
	v_lshl_add_u64 v[36:37], s[2:3], 0, v[38:39]
	global_store_dword v[40:41], v9, off
	global_store_dword v[36:37], v5, off
.LBB0_846:
	s_or_b64 exec, exec, s[4:5]
	v_mov_b32_e32 v217, v3
	s_and_saveexec_b64 s[4:5], s[66:67]
	s_xor_b64 s[4:5], exec, s[4:5]
	v_cmp_lt_i32_e64 s[24:25], v2, v11
	v_sub_u32_e32 v3, v2, v11
	v_add_u32_e32 v3, 0x400, v3
	v_cndmask_b32_e64 v5, 0, 1, s[60:61]
	s_and_b64 s[24:25], s[60:61], s[24:25]
	v_add_u32_e32 v2, v2, v5
	v_cndmask_b32_e64 v5, -1, v3, s[24:25]
	s_or_saveexec_b64 s[4:5], s[4:5]
	v_mov_b32_e32 v3, v4
	s_xor_b64 exec, exec, s[4:5]
	v_add_u32_e32 v3, 1, v4
	v_mov_b32_e32 v5, v4
	s_or_b64 exec, exec, s[4:5]
	v_add3_u32 v9, s68, v8, 2
	v_mov_b32_e32 v4, -1
	v_cmp_lt_i32_e64 s[24:25], -1, v5
	s_and_saveexec_b64 s[4:5], s[24:25]
	s_cbranch_execz .LBB0_852
	v_add_u32_e32 v4, s55, v5
	v_add_u32_e32 v36, s54, v4
	v_ashrrev_i32_e32 v37, 31, v36
	v_lshlrev_b64 v[36:37], 2, v[36:37]
	v_lshl_add_u64 v[38:39], s[84:85], 0, v[36:37]
	v_lshrrev_b32_e32 v5, 2, v35
	v_lshl_add_u64 v[36:37], s[2:3], 0, v[36:37]
	global_store_dword v[38:39], v9, off
	global_store_dword v[36:37], v5, off
.LBB0_852:
	s_or_b64 exec, exec, s[4:5]
	v_mov_b32_e32 v218, v4
	s_and_saveexec_b64 s[4:5], s[62:63]
	s_xor_b64 s[4:5], exec, s[4:5]
	v_cmp_lt_i32_e64 s[24:25], v2, v11
	v_sub_u32_e32 v4, v2, v11
	v_add_u32_e32 v4, 0x400, v4
	v_cndmask_b32_e64 v5, 0, 1, s[56:57]
	s_and_b64 s[24:25], s[56:57], s[24:25]
	v_add_u32_e32 v2, v2, v5
	v_cndmask_b32_e64 v5, -1, v4, s[24:25]
	s_or_saveexec_b64 s[4:5], s[4:5]
	v_mov_b32_e32 v4, v3
	s_xor_b64 exec, exec, s[4:5]
	v_add_u32_e32 v4, 1, v3
	v_mov_b32_e32 v5, v3
	s_or_b64 exec, exec, s[4:5]
	v_add3_u32 v9, s68, v8, 3
	v_mov_b32_e32 v3, -1
	v_cmp_lt_i32_e64 s[24:25], -1, v5
	s_and_saveexec_b64 s[4:5], s[24:25]
	s_cbranch_execz .LBB0_858
	v_add_u32_e32 v3, s55, v5
	v_add_u32_e32 v36, s54, v3
	v_ashrrev_i32_e32 v37, 31, v36
	v_lshlrev_b64 v[36:37], 2, v[36:37]
	v_lshl_add_u64 v[38:39], s[84:85], 0, v[36:37]
	v_lshrrev_b32_e32 v5, 2, v34
	v_lshl_add_u64 v[34:35], s[2:3], 0, v[36:37]
	global_store_dword v[38:39], v9, off
	global_store_dword v[34:35], v5, off
.LBB0_858:
	s_or_b64 exec, exec, s[4:5]
	v_mov_b32_e32 v219, v3
	s_and_saveexec_b64 s[4:5], s[58:59]
	s_xor_b64 s[4:5], exec, s[4:5]
	v_cmp_lt_i32_e64 s[24:25], v2, v11
	v_sub_u32_e32 v3, v2, v11
	v_add_u32_e32 v3, 0x400, v3
	v_cndmask_b32_e64 v5, 0, 1, s[48:49]
	s_and_b64 s[24:25], s[48:49], s[24:25]
	v_add_u32_e32 v2, v2, v5
	v_cndmask_b32_e64 v5, -1, v3, s[24:25]
	s_or_saveexec_b64 s[4:5], s[4:5]
	v_mov_b32_e32 v3, v4
	s_xor_b64 exec, exec, s[4:5]
	v_add_u32_e32 v3, 1, v4
	v_mov_b32_e32 v5, v4
	s_or_b64 exec, exec, s[4:5]
	v_add3_u32 v9, s68, v8, 4
	v_mov_b32_e32 v4, -1
	v_cmp_lt_i32_e64 s[24:25], -1, v5
	s_and_saveexec_b64 s[4:5], s[24:25]
	s_cbranch_execz .LBB0_864
	v_add_u32_e32 v4, s55, v5
	v_add_u32_e32 v34, s54, v4
	v_ashrrev_i32_e32 v35, 31, v34
	v_lshlrev_b64 v[34:35], 2, v[34:35]
	v_lshl_add_u64 v[36:37], s[84:85], 0, v[34:35]
	v_lshrrev_b32_e32 v5, 2, v33
	v_lshl_add_u64 v[34:35], s[2:3], 0, v[34:35]
	global_store_dword v[36:37], v9, off
	global_store_dword v[34:35], v5, off
.LBB0_864:
	s_or_b64 exec, exec, s[4:5]
	v_mov_b32_e32 v220, v4
	s_and_saveexec_b64 s[4:5], s[50:51]
	s_xor_b64 s[4:5], exec, s[4:5]
	v_cmp_lt_i32_e64 s[24:25], v2, v11
	v_sub_u32_e32 v4, v2, v11
	v_add_u32_e32 v4, 0x400, v4
	v_cndmask_b32_e64 v5, 0, 1, s[44:45]
	s_and_b64 s[24:25], s[44:45], s[24:25]
	v_add_u32_e32 v2, v2, v5
	v_cndmask_b32_e64 v5, -1, v4, s[24:25]
	s_or_saveexec_b64 s[4:5], s[4:5]
	v_mov_b32_e32 v4, v3
	s_xor_b64 exec, exec, s[4:5]
	v_add_u32_e32 v4, 1, v3
	v_mov_b32_e32 v5, v3
	s_or_b64 exec, exec, s[4:5]
	v_add3_u32 v9, s68, v8, 5
	v_mov_b32_e32 v3, -1
	v_cmp_lt_i32_e64 s[24:25], -1, v5
	s_and_saveexec_b64 s[4:5], s[24:25]
	s_cbranch_execz .LBB0_870
	v_add_u32_e32 v3, s55, v5
	v_add_u32_e32 v34, s54, v3
	v_ashrrev_i32_e32 v35, 31, v34
	v_lshlrev_b64 v[34:35], 2, v[34:35]
	v_lshl_add_u64 v[36:37], s[84:85], 0, v[34:35]
	v_lshrrev_b32_e32 v5, 2, v32
	v_lshl_add_u64 v[32:33], s[2:3], 0, v[34:35]
	global_store_dword v[36:37], v9, off
	global_store_dword v[32:33], v5, off
.LBB0_870:
	s_or_b64 exec, exec, s[4:5]
	v_mov_b32_e32 v221, v3
	s_and_saveexec_b64 s[4:5], s[46:47]
	s_xor_b64 s[4:5], exec, s[4:5]
	v_cmp_lt_i32_e64 s[24:25], v2, v11
	v_sub_u32_e32 v3, v2, v11
	v_add_u32_e32 v3, 0x400, v3
	v_cndmask_b32_e64 v5, 0, 1, s[40:41]
	s_and_b64 s[24:25], s[40:41], s[24:25]
	v_add_u32_e32 v2, v2, v5
	v_cndmask_b32_e64 v5, -1, v3, s[24:25]
	s_or_saveexec_b64 s[4:5], s[4:5]
	v_mov_b32_e32 v3, v4
	s_xor_b64 exec, exec, s[4:5]
	v_add_u32_e32 v3, 1, v4
	v_mov_b32_e32 v5, v4
	s_or_b64 exec, exec, s[4:5]
	v_add3_u32 v9, s68, v8, 6
	v_mov_b32_e32 v4, -1
	v_cmp_lt_i32_e64 s[24:25], -1, v5
	s_and_saveexec_b64 s[4:5], s[24:25]
	s_cbranch_execz .LBB0_876
	v_add_u32_e32 v4, s55, v5
	v_add_u32_e32 v32, s54, v4
	v_ashrrev_i32_e32 v33, 31, v32
	v_lshlrev_b64 v[32:33], 2, v[32:33]
	v_lshl_add_u64 v[34:35], s[84:85], 0, v[32:33]
	v_lshrrev_b32_e32 v5, 2, v31
	v_lshl_add_u64 v[32:33], s[2:3], 0, v[32:33]
	global_store_dword v[34:35], v9, off
	global_store_dword v[32:33], v5, off
; template <int VPT>
; __device__ __forceinline__ void topk_list(const Params& p, LAS unsigned char* lds, const float* a, int N, int cap, int rowbase, int mbase, int e) {
;     ...
;     if (active) {
; #pragma unroll
;         for (int j = 0; j < VPT; ++j) {
;             const int i = tid * VPT + j, row = rowbase + i; int slot = -1;
;             if (k[j] > T) slot = gtb++;
;             else if (k[j] == T) { if (eqb < need) slot = G + eqb; ++eqb; }
;             if (slot >= 0) { const int m = mbase + slot; WSP(int, OFF_RIDX)[e * MEXP + m] = row; WSP(float, OFF_GATE)[e * MEXP + m] = __uint_as_float(k[j] >> 2); WSP(int, OFF_SLOT)[row * 16 + e] = m; }
;             else WSP(int, OFF_SLOT)[row * 16 + e] = -1;
;         }
.LBB0_876:
	s_or_b64 exec, exec, s[4:5]
	v_mov_b32_e32 v222, v4
	s_and_saveexec_b64 s[4:5], s[42:43]
	s_xor_b64 s[4:5], exec, s[4:5]
	v_cmp_lt_i32_e64 s[24:25], v2, v11
	v_sub_u32_e32 v4, v2, v11
	v_add_u32_e32 v4, 0x400, v4
	v_cndmask_b32_e64 v5, 0, 1, s[36:37]
	s_and_b64 s[24:25], s[36:37], s[24:25]
	v_add_u32_e32 v2, v2, v5
	v_cndmask_b32_e64 v5, -1, v4, s[24:25]
	s_or_saveexec_b64 s[4:5], s[4:5]
	v_mov_b32_e32 v4, v3
	s_xor_b64 exec, exec, s[4:5]
	v_add_u32_e32 v4, 1, v3
	v_mov_b32_e32 v5, v3
	s_or_b64 exec, exec, s[4:5]
	v_add3_u32 v9, s68, v8, 7
	v_mov_b32_e32 v3, -1
	v_cmp_lt_i32_e64 s[24:25], -1, v5
	s_and_saveexec_b64 s[4:5], s[24:25]
	s_cbranch_execz .LBB0_882
	v_add_u32_e32 v3, s55, v5
	v_add_u32_e32 v32, s54, v3
	v_ashrrev_i32_e32 v33, 31, v32
	v_lshlrev_b64 v[32:33], 2, v[32:33]
	v_lshl_add_u64 v[34:35], s[84:85], 0, v[32:33]
	v_lshrrev_b32_e32 v5, 2, v30
	v_lshl_add_u64 v[30:31], s[2:3], 0, v[32:33]
	global_store_dword v[34:35], v9, off
	global_store_dword v[30:31], v5, off
.LBB0_882:
	s_or_b64 exec, exec, s[4:5]
	v_mov_b32_e32 v223, v3
	s_and_saveexec_b64 s[4:5], s[38:39]
	s_xor_b64 s[4:5], exec, s[4:5]
	v_cmp_lt_i32_e64 s[24:25], v2, v11
	v_sub_u32_e32 v3, v2, v11
	v_add_u32_e32 v3, 0x400, v3
	v_cndmask_b32_e64 v5, 0, 1, s[30:31]
	s_and_b64 s[24:25], s[30:31], s[24:25]
	v_add_u32_e32 v2, v2, v5
	v_cndmask_b32_e64 v5, -1, v3, s[24:25]
	s_or_saveexec_b64 s[4:5], s[4:5]
	v_mov_b32_e32 v3, v4
	s_xor_b64 exec, exec, s[4:5]
	v_add_u32_e32 v3, 1, v4
	v_mov_b32_e32 v5, v4
	s_or_b64 exec, exec, s[4:5]
	v_add3_u32 v9, s68, v8, 8
	v_mov_b32_e32 v4, -1
	v_cmp_lt_i32_e64 s[24:25], -1, v5
	s_and_saveexec_b64 s[4:5], s[24:25]
	s_cbranch_execz .LBB0_888
	v_add_u32_e32 v4, s55, v5
	v_add_u32_e32 v30, s54, v4
	v_ashrrev_i32_e32 v31, 31, v30
	v_lshlrev_b64 v[30:31], 2, v[30:31]
	v_lshl_add_u64 v[32:33], s[84:85], 0, v[30:31]
	v_lshrrev_b32_e32 v5, 2, v29
	v_lshl_add_u64 v[30:31], s[2:3], 0, v[30:31]
	global_store_dword v[32:33], v9, off
	global_store_dword v[30:31], v5, off
.LBB0_888:
	s_or_b64 exec, exec, s[4:5]
	v_mov_b32_e32 v224, v4
	s_and_saveexec_b64 s[4:5], s[34:35]
	s_xor_b64 s[4:5], exec, s[4:5]
	v_cmp_lt_i32_e64 s[24:25], v2, v11
	v_sub_u32_e32 v4, v2, v11
	v_add_u32_e32 v4, 0x400, v4
	v_cndmask_b32_e64 v5, 0, 1, s[26:27]
	s_and_b64 s[24:25], s[26:27], s[24:25]
	v_add_u32_e32 v2, v2, v5
	v_cndmask_b32_e64 v5, -1, v4, s[24:25]
	s_or_saveexec_b64 s[4:5], s[4:5]
	v_mov_b32_e32 v4, v3
	s_xor_b64 exec, exec, s[4:5]
	v_add_u32_e32 v4, 1, v3
	v_mov_b32_e32 v5, v3
	s_or_b64 exec, exec, s[4:5]
	v_add3_u32 v9, s68, v8, 9
	v_mov_b32_e32 v3, -1
	v_cmp_lt_i32_e64 s[24:25], -1, v5
	s_and_saveexec_b64 s[4:5], s[24:25]
	s_cbranch_execz .LBB0_894
	v_add_u32_e32 v3, s55, v5
	v_add_u32_e32 v30, s54, v3
	v_ashrrev_i32_e32 v31, 31, v30
	v_lshlrev_b64 v[30:31], 2, v[30:31]
	v_lshl_add_u64 v[32:33], s[84:85], 0, v[30:31]
	v_lshrrev_b32_e32 v5, 2, v28
	v_lshl_add_u64 v[28:29], s[2:3], 0, v[30:31]
	global_store_dword v[32:33], v9, off
	global_store_dword v[28:29], v5, off
.LBB0_894:
	s_or_b64 exec, exec, s[4:5]
	v_mov_b32_e32 v225, v3
	s_and_saveexec_b64 s[4:5], s[28:29]
	s_xor_b64 s[4:5], exec, s[4:5]
	v_cmp_lt_i32_e64 s[24:25], v2, v11
	v_sub_u32_e32 v3, v2, v11
	v_add_u32_e32 v3, 0x400, v3
	v_cndmask_b32_e64 v5, 0, 1, s[20:21]
	s_and_b64 s[20:21], s[20:21], s[24:25]
	v_add_u32_e32 v2, v2, v5
	v_cndmask_b32_e64 v5, -1, v3, s[20:21]
	s_or_saveexec_b64 s[4:5], s[4:5]
	v_mov_b32_e32 v3, v4
	s_xor_b64 exec, exec, s[4:5]
	v_add_u32_e32 v3, 1, v4
	v_mov_b32_e32 v5, v4
	s_or_b64 exec, exec, s[4:5]
	v_add3_u32 v9, s68, v8, 10
	v_mov_b32_e32 v4, -1
	v_cmp_lt_i32_e64 s[20:21], -1, v5
	s_and_saveexec_b64 s[4:5], s[20:21]
	s_cbranch_execz .LBB0_900
	v_add_u32_e32 v4, s55, v5
	v_add_u32_e32 v28, s54, v4
	v_ashrrev_i32_e32 v29, 31, v28
	v_lshlrev_b64 v[28:29], 2, v[28:29]
	v_lshl_add_u64 v[30:31], s[84:85], 0, v[28:29]
	v_lshrrev_b32_e32 v5, 2, v27
	v_lshl_add_u64 v[28:29], s[2:3], 0, v[28:29]
	global_store_dword v[30:31], v9, off
	global_store_dword v[28:29], v5, off
.LBB0_900:
	s_or_b64 exec, exec, s[4:5]
	v_mov_b32_e32 v226, v4
	s_and_saveexec_b64 s[4:5], s[22:23]
	s_xor_b64 s[4:5], exec, s[4:5]
	v_cmp_lt_i32_e64 s[20:21], v2, v11
	v_sub_u32_e32 v4, v2, v11
	v_add_u32_e32 v4, 0x400, v4
	v_cndmask_b32_e64 v5, 0, 1, s[16:17]
	s_and_b64 s[16:17], s[16:17], s[20:21]
	v_add_u32_e32 v2, v2, v5
	v_cndmask_b32_e64 v5, -1, v4, s[16:17]
	s_or_saveexec_b64 s[4:5], s[4:5]
	v_mov_b32_e32 v4, v3
	s_xor_b64 exec, exec, s[4:5]
	v_add_u32_e32 v4, 1, v3
	v_mov_b32_e32 v5, v3
	s_or_b64 exec, exec, s[4:5]
	v_add3_u32 v9, s68, v8, 11
	v_mov_b32_e32 v3, -1
	v_cmp_lt_i32_e64 s[16:17], -1, v5
	s_and_saveexec_b64 s[4:5], s[16:17]
	s_cbranch_execz .LBB0_906
	v_add_u32_e32 v3, s55, v5
	v_add_u32_e32 v28, s54, v3
	v_ashrrev_i32_e32 v29, 31, v28
	v_lshlrev_b64 v[28:29], 2, v[28:29]
	v_lshl_add_u64 v[30:31], s[84:85], 0, v[28:29]
	v_lshrrev_b32_e32 v5, 2, v26
	v_lshl_add_u64 v[26:27], s[2:3], 0, v[28:29]
	global_store_dword v[30:31], v9, off
	global_store_dword v[26:27], v5, off
; template <int VPT>
; __device__ __forceinline__ void topk_list(const Params& p, LAS unsigned char* lds, const float* a, int N, int cap, int rowbase, int mbase, int e) {
;     ...
;     if (active) {
; #pragma unroll
;         for (int j = 0; j < VPT; ++j) {
;             const int i = tid * VPT + j, row = rowbase + i; int slot = -1;
;             if (k[j] > T) slot = gtb++;
;             else if (k[j] == T) { if (eqb < need) slot = G + eqb; ++eqb; }
;             if (slot >= 0) { const int m = mbase + slot; WSP(int, OFF_RIDX)[e * MEXP + m] = row; WSP(float, OFF_GATE)[e * MEXP + m] = __uint_as_float(k[j] >> 2); WSP(int, OFF_SLOT)[row * 16 + e] = m; }
;             else WSP(int, OFF_SLOT)[row * 16 + e] = -1;
;         }
.LBB0_906:
	s_or_b64 exec, exec, s[4:5]
	v_mov_b32_e32 v227, v3
	s_and_saveexec_b64 s[4:5], s[18:19]
	s_xor_b64 s[4:5], exec, s[4:5]
	v_cmp_lt_i32_e64 s[16:17], v2, v11
	v_sub_u32_e32 v3, v2, v11
	v_add_u32_e32 v3, 0x400, v3
	v_cndmask_b32_e64 v5, 0, 1, s[12:13]
	s_and_b64 s[12:13], s[12:13], s[16:17]
	v_add_u32_e32 v2, v2, v5
	v_cndmask_b32_e64 v5, -1, v3, s[12:13]
	s_or_saveexec_b64 s[4:5], s[4:5]
	v_mov_b32_e32 v3, v4
	s_xor_b64 exec, exec, s[4:5]
	v_add_u32_e32 v3, 1, v4
	v_mov_b32_e32 v5, v4
	s_or_b64 exec, exec, s[4:5]
	v_add3_u32 v9, s68, v8, 12
	v_mov_b32_e32 v4, -1
	v_cmp_lt_i32_e64 s[12:13], -1, v5
	s_and_saveexec_b64 s[4:5], s[12:13]
	s_cbranch_execz .LBB0_912
	v_add_u32_e32 v4, s55, v5
	v_add_u32_e32 v26, s54, v4
	v_ashrrev_i32_e32 v27, 31, v26
	v_lshlrev_b64 v[26:27], 2, v[26:27]
	v_lshl_add_u64 v[28:29], s[84:85], 0, v[26:27]
	v_lshrrev_b32_e32 v5, 2, v25
	v_lshl_add_u64 v[26:27], s[2:3], 0, v[26:27]
	global_store_dword v[28:29], v9, off
	global_store_dword v[26:27], v5, off
.LBB0_912:
	s_or_b64 exec, exec, s[4:5]
	v_mov_b32_e32 v228, v4
	s_and_saveexec_b64 s[4:5], s[14:15]
	s_xor_b64 s[4:5], exec, s[4:5]
	v_cmp_lt_i32_e64 s[12:13], v2, v11
	v_sub_u32_e32 v4, v2, v11
	v_add_u32_e32 v4, 0x400, v4
	v_cndmask_b32_e64 v5, 0, 1, s[8:9]
	s_and_b64 s[8:9], s[8:9], s[12:13]
	v_add_u32_e32 v2, v2, v5
	v_cndmask_b32_e64 v5, -1, v4, s[8:9]
	s_or_saveexec_b64 s[4:5], s[4:5]
	v_mov_b32_e32 v4, v3
	s_xor_b64 exec, exec, s[4:5]
	v_add_u32_e32 v4, 1, v3
	v_mov_b32_e32 v5, v3
	s_or_b64 exec, exec, s[4:5]
	v_add3_u32 v9, s68, v8, 13
	v_mov_b32_e32 v3, -1
	v_cmp_lt_i32_e64 s[8:9], -1, v5
	s_and_saveexec_b64 s[4:5], s[8:9]
	s_cbranch_execz .LBB0_918
	v_add_u32_e32 v3, s55, v5
	v_add_u32_e32 v26, s54, v3
	v_ashrrev_i32_e32 v27, 31, v26
	v_lshlrev_b64 v[26:27], 2, v[26:27]
	v_lshl_add_u64 v[28:29], s[84:85], 0, v[26:27]
	v_lshrrev_b32_e32 v5, 2, v24
	v_lshl_add_u64 v[24:25], s[2:3], 0, v[26:27]
	global_store_dword v[28:29], v9, off
	global_store_dword v[24:25], v5, off
.LBB0_918:
	s_or_b64 exec, exec, s[4:5]
	v_mov_b32_e32 v229, v3
	s_and_saveexec_b64 s[4:5], s[10:11]
	s_xor_b64 s[4:5], exec, s[4:5]
	v_cmp_lt_i32_e64 s[8:9], v2, v11
	v_sub_u32_e32 v3, v2, v11
	v_add_u32_e32 v3, 0x400, v3
	v_cndmask_b32_e64 v5, 0, 1, s[6:7]
	s_and_b64 s[6:7], s[6:7], s[8:9]
	v_add_u32_e32 v2, v2, v5
	v_cndmask_b32_e64 v9, -1, v3, s[6:7]
	s_or_saveexec_b64 s[4:5], s[4:5]
	v_mov_b32_e32 v5, v4
	s_xor_b64 exec, exec, s[4:5]
	v_add_u32_e32 v5, 1, v4
	v_mov_b32_e32 v9, v4
	s_or_b64 exec, exec, s[4:5]
	v_add3_u32 v10, s68, v8, 14
	v_mov_b32_e32 v3, -1
	v_cmp_lt_i32_e64 s[6:7], -1, v9
	v_mov_b32_e32 v4, -1
	s_and_saveexec_b64 s[4:5], s[6:7]
	s_cbranch_execz .LBB0_924
	v_add_u32_e32 v4, s55, v9
	v_add_u32_e32 v24, s54, v4
	v_ashrrev_i32_e32 v25, 31, v24
	v_lshlrev_b64 v[24:25], 2, v[24:25]
	v_lshl_add_u64 v[26:27], s[84:85], 0, v[24:25]
	v_lshrrev_b32_e32 v9, 2, v23
	v_lshl_add_u64 v[24:25], s[2:3], 0, v[24:25]
	global_store_dword v[26:27], v10, off
	global_store_dword v[24:25], v9, off
.LBB0_924:
	s_or_b64 exec, exec, s[4:5]
	v_cmp_lt_i32_e64 s[6:7], v2, v11
	v_sub_u32_e32 v2, v2, v11
	v_add_u32_e32 v2, 0x400, v2
	s_and_b64 s[0:1], s[0:1], s[6:7]
	v_cndmask_b32_e64 v2, -1, v2, s[0:1]
	v_cndmask_b32_e32 v2, v2, v5, vcc
	v_mov_b32_e32 v230, v4
	v_add3_u32 v4, s68, v8, 15
	v_cmp_lt_i32_e32 vcc, -1, v2
	s_and_saveexec_b64 s[0:1], vcc
	s_cbranch_execz .LBB0_926
	v_add_u32_e32 v3, s55, v2
	v_add_u32_e32 v8, s54, v3
	v_ashrrev_i32_e32 v9, 31, v8
	v_lshlrev_b64 v[8:9], 2, v[8:9]
	v_lshl_add_u64 v[10:11], s[84:85], 0, v[8:9]
	v_lshrrev_b32_e32 v2, 2, v6
	v_lshl_add_u64 v[8:9], s[2:3], 0, v[8:9]
	global_store_dword v[10:11], v4, off
	global_store_dword v[8:9], v2, off
.LBB0_926:
	s_or_b64 exec, exec, s[0:1]
	v_mov_b32_e32 v231, v3
	s_mul_i32 s98, s92, 0x4200
	v_subrev_u32_e32 v4, 15, v4
	v_add_u32_e32 v4, s98, v4
	v_ashrrev_i32_e32 v5, 31, v4
	v_lshl_add_u64 v[4:5], v[4:5], 2, s[80:81]
	global_store_dwordx4 v[4:5], v[216:219], off
	global_store_dwordx4 v[4:5], v[220:223], off offset:16
	global_store_dwordx4 v[4:5], v[224:227], off offset:32
	global_store_dwordx4 v[4:5], v[228:231], off offset:48

; template <int VPT>
; __device__ __forceinline__ void topk_list(const Params& p, LAS unsigned char* lds, const float* a, int N, int cap, int rowbase, int mbase, int e) {
;     ...
;     if (active) {
; #pragma unroll
;         for (int j = 0; j < VPT; ++j) {
;             const int i = tid * VPT + j, row = rowbase + i; int slot = -1;
;             if (k[j] > T) slot = gtb++;
;             else if (k[j] == T) { if (eqb < need) slot = G + eqb; ++eqb; }
;             if (slot >= 0) { const int m = mbase + slot; WSP(int, OFF_RIDX)[e * MEXP + m] = row; WSP(float, OFF_GATE)[e * MEXP + m] = __uint_as_float(k[j] >> 2); WSP(int, OFF_SLOT)[row * 16 + e] = m; }
;             else WSP(int, OFF_SLOT)[row * 16 + e] = -1;
;         }
.LBB0_2175:
	s_or_b64 exec, exec, s[52:53]
	v_mov_b32_e32 v216, v5
	s_and_saveexec_b64 s[22:23], s[68:69]
	s_xor_b64 s[52:53], exec, s[22:23]
	v_cmp_lt_i32_e64 s[22:23], v2, v9
	v_sub_u32_e32 v4, v2, v9
	v_add_u32_e32 v4, 0x400, v4
	v_cndmask_b32_e64 v5, 0, 1, s[62:63]
	s_and_b64 s[22:23], s[62:63], s[22:23]
	v_add_u32_e32 v2, v2, v5
	v_cndmask_b32_e64 v5, -1, v4, s[22:23]
	s_or_saveexec_b64 s[22:23], s[52:53]
	v_mov_b32_e32 v4, v3
	s_xor_b64 exec, exec, s[22:23]
	v_add_u32_e32 v4, 1, v3
	v_mov_b32_e32 v5, v3
	s_or_b64 exec, exec, s[22:23]
	v_add3_u32 v8, s70, v6, 1
	v_mov_b32_e32 v3, -1
	v_cmp_lt_i32_e64 s[22:23], -1, v5
	s_and_saveexec_b64 s[52:53], s[22:23]
	s_cbranch_execz .LBB0_2181
	v_add_u32_e32 v3, s67, v5
	v_add_u32_e32 v28, s66, v3
	v_ashrrev_i32_e32 v29, 31, v28
	v_lshlrev_b64 v[28:29], 2, v[28:29]
	v_lshl_add_u64 v[30:31], s[96:97], 0, v[28:29]
	v_lshl_add_u64 v[28:29], s[80:81], 0, v[28:29]
	v_lshrrev_b32_e32 v5, 2, v27
	global_store_dword v[28:29], v8, off
	global_store_dword v[30:31], v5, off
.LBB0_2181:
	s_or_b64 exec, exec, s[52:53]
	v_mov_b32_e32 v217, v3
	s_and_saveexec_b64 s[22:23], s[64:65]
	s_xor_b64 s[52:53], exec, s[22:23]
	v_cmp_lt_i32_e64 s[22:23], v2, v9
	v_sub_u32_e32 v3, v2, v9
	v_add_u32_e32 v3, 0x400, v3
	v_cndmask_b32_e64 v5, 0, 1, s[58:59]
	s_and_b64 s[22:23], s[58:59], s[22:23]
	v_add_u32_e32 v2, v2, v5
	v_cndmask_b32_e64 v5, -1, v3, s[22:23]
	s_or_saveexec_b64 s[22:23], s[52:53]
	v_mov_b32_e32 v3, v4
	s_xor_b64 exec, exec, s[22:23]
	v_add_u32_e32 v3, 1, v4
	v_mov_b32_e32 v5, v4
	s_or_b64 exec, exec, s[22:23]
	v_add3_u32 v8, s70, v6, 2
	v_mov_b32_e32 v4, -1
	v_cmp_lt_i32_e64 s[22:23], -1, v5
	s_and_saveexec_b64 s[52:53], s[22:23]
	s_cbranch_execz .LBB0_2187
	v_add_u32_e32 v4, s67, v5
	v_add_u32_e32 v28, s66, v4
	v_ashrrev_i32_e32 v29, 31, v28
	v_lshlrev_b64 v[28:29], 2, v[28:29]
	v_lshrrev_b32_e32 v5, 2, v26
	v_lshl_add_u64 v[26:27], s[80:81], 0, v[28:29]
	v_lshl_add_u64 v[30:31], s[96:97], 0, v[28:29]
	global_store_dword v[26:27], v8, off
	global_store_dword v[30:31], v5, off
.LBB0_2187:
	s_or_b64 exec, exec, s[52:53]
	v_mov_b32_e32 v218, v4
	s_and_saveexec_b64 s[22:23], s[60:61]
	s_xor_b64 s[52:53], exec, s[22:23]
	v_cmp_lt_i32_e64 s[22:23], v2, v9
	v_sub_u32_e32 v4, v2, v9
	v_add_u32_e32 v4, 0x400, v4
	v_cndmask_b32_e64 v5, 0, 1, s[54:55]
	s_and_b64 s[22:23], s[54:55], s[22:23]
	v_add_u32_e32 v2, v2, v5
	v_cndmask_b32_e64 v5, -1, v4, s[22:23]
	s_or_saveexec_b64 s[22:23], s[52:53]
	v_mov_b32_e32 v4, v3
	s_xor_b64 exec, exec, s[22:23]
	v_add_u32_e32 v4, 1, v3
	v_mov_b32_e32 v5, v3
	s_or_b64 exec, exec, s[22:23]
	v_add3_u32 v8, s70, v6, 3
	v_mov_b32_e32 v3, -1
	v_cmp_lt_i32_e64 s[22:23], -1, v5
	s_and_saveexec_b64 s[52:53], s[22:23]
	s_cbranch_execz .LBB0_2193
	v_add_u32_e32 v3, s67, v5
	v_add_u32_e32 v26, s66, v3
	v_ashrrev_i32_e32 v27, 31, v26
	v_lshlrev_b64 v[26:27], 2, v[26:27]
	v_lshl_add_u64 v[28:29], s[96:97], 0, v[26:27]
	v_lshl_add_u64 v[26:27], s[80:81], 0, v[26:27]
	v_lshrrev_b32_e32 v5, 2, v25
	global_store_dword v[26:27], v8, off
	global_store_dword v[28:29], v5, off
.LBB0_2193:
	s_or_b64 exec, exec, s[52:53]
	v_mov_b32_e32 v219, v3
	s_and_saveexec_b64 s[22:23], s[56:57]
	s_xor_b64 s[52:53], exec, s[22:23]
	v_cmp_lt_i32_e64 s[22:23], v2, v9
	v_sub_u32_e32 v3, v2, v9
	v_add_u32_e32 v3, 0x400, v3
	v_cndmask_b32_e64 v5, 0, 1, s[46:47]
	s_and_b64 s[22:23], s[46:47], s[22:23]
	v_add_u32_e32 v2, v2, v5
	v_cndmask_b32_e64 v5, -1, v3, s[22:23]
	s_or_saveexec_b64 s[22:23], s[52:53]
	v_mov_b32_e32 v3, v4
	s_xor_b64 exec, exec, s[22:23]
	v_add_u32_e32 v3, 1, v4
	v_mov_b32_e32 v5, v4
	s_or_b64 exec, exec, s[22:23]
	v_add3_u32 v8, s70, v6, 4
	v_mov_b32_e32 v4, -1
	v_cmp_lt_i32_e64 s[22:23], -1, v5
	s_and_saveexec_b64 s[46:47], s[22:23]
	s_cbranch_execz .LBB0_2199
	v_add_u32_e32 v4, s67, v5
	v_add_u32_e32 v26, s66, v4
	v_ashrrev_i32_e32 v27, 31, v26
	v_lshlrev_b64 v[26:27], 2, v[26:27]
	v_lshrrev_b32_e32 v5, 2, v24
	v_lshl_add_u64 v[24:25], s[80:81], 0, v[26:27]
	v_lshl_add_u64 v[28:29], s[96:97], 0, v[26:27]
	global_store_dword v[24:25], v8, off
	global_store_dword v[28:29], v5, off
.LBB0_2199:
	s_or_b64 exec, exec, s[46:47]
	v_mov_b32_e32 v220, v4
	s_and_saveexec_b64 s[22:23], s[50:51]
	s_xor_b64 s[46:47], exec, s[22:23]
	v_cmp_lt_i32_e64 s[22:23], v2, v9
	v_sub_u32_e32 v4, v2, v9
	v_add_u32_e32 v4, 0x400, v4
	v_cndmask_b32_e64 v5, 0, 1, s[42:43]
	s_and_b64 s[22:23], s[42:43], s[22:23]
	v_add_u32_e32 v2, v2, v5
	v_cndmask_b32_e64 v5, -1, v4, s[22:23]
	s_or_saveexec_b64 s[22:23], s[46:47]
	v_mov_b32_e32 v4, v3
	s_xor_b64 exec, exec, s[22:23]
	v_add_u32_e32 v4, 1, v3
	v_mov_b32_e32 v5, v3
	s_or_b64 exec, exec, s[22:23]
	v_add3_u32 v8, s70, v6, 5
	v_mov_b32_e32 v3, -1
	v_cmp_lt_i32_e64 s[22:23], -1, v5
	s_and_saveexec_b64 s[42:43], s[22:23]
	s_cbranch_execz .LBB0_2205
	v_add_u32_e32 v3, s67, v5
	v_add_u32_e32 v24, s66, v3
	v_ashrrev_i32_e32 v25, 31, v24
	v_lshlrev_b64 v[24:25], 2, v[24:25]
	v_lshl_add_u64 v[26:27], s[96:97], 0, v[24:25]
	v_lshl_add_u64 v[24:25], s[80:81], 0, v[24:25]
	v_lshrrev_b32_e32 v5, 2, v23
	global_store_dword v[24:25], v8, off
	global_store_dword v[26:27], v5, off
.LBB0_2205:
	s_or_b64 exec, exec, s[42:43]
	v_mov_b32_e32 v221, v3
	s_and_saveexec_b64 s[22:23], s[44:45]
	s_xor_b64 s[42:43], exec, s[22:23]
	v_cmp_lt_i32_e64 s[22:23], v2, v9
	v_sub_u32_e32 v3, v2, v9
	v_add_u32_e32 v3, 0x400, v3
	v_cndmask_b32_e64 v5, 0, 1, s[38:39]
	s_and_b64 s[22:23], s[38:39], s[22:23]
	v_add_u32_e32 v2, v2, v5
	v_cndmask_b32_e64 v5, -1, v3, s[22:23]
	s_or_saveexec_b64 s[22:23], s[42:43]
	v_mov_b32_e32 v3, v4
	s_xor_b64 exec, exec, s[22:23]
	v_add_u32_e32 v3, 1, v4
	v_mov_b32_e32 v5, v4
	s_or_b64 exec, exec, s[22:23]
	v_add3_u32 v8, s70, v6, 6
	v_mov_b32_e32 v4, -1
	v_cmp_lt_i32_e64 s[22:23], -1, v5
	s_and_saveexec_b64 s[38:39], s[22:23]
	s_cbranch_execz .LBB0_2211
	v_add_u32_e32 v4, s67, v5
	v_add_u32_e32 v24, s66, v4
	v_ashrrev_i32_e32 v25, 31, v24
	v_lshlrev_b64 v[24:25], 2, v[24:25]
	v_lshrrev_b32_e32 v5, 2, v22
	v_lshl_add_u64 v[22:23], s[80:81], 0, v[24:25]
	v_lshl_add_u64 v[26:27], s[96:97], 0, v[24:25]
	global_store_dword v[22:23], v8, off
	global_store_dword v[26:27], v5, off
; template <int VPT>
; __device__ __forceinline__ void topk_list(const Params& p, LAS unsigned char* lds, const float* a, int N, int cap, int rowbase, int mbase, int e) {
;     ...
;     if (active) {
; #pragma unroll
;         for (int j = 0; j < VPT; ++j) {
;             const int i = tid * VPT + j, row = rowbase + i; int slot = -1;
;             if (k[j] > T) slot = gtb++;
;             else if (k[j] == T) { if (eqb < need) slot = G + eqb; ++eqb; }
;             if (slot >= 0) { const int m = mbase + slot; WSP(int, OFF_RIDX)[e * MEXP + m] = row; WSP(float, OFF_GATE)[e * MEXP + m] = __uint_as_float(k[j] >> 2); WSP(int, OFF_SLOT)[row * 16 + e] = m; }
;             else WSP(int, OFF_SLOT)[row * 16 + e] = -1;
;         }
.LBB0_2211:
	s_or_b64 exec, exec, s[38:39]
	v_mov_b32_e32 v222, v4
	s_and_saveexec_b64 s[22:23], s[40:41]
	s_xor_b64 s[38:39], exec, s[22:23]
	v_cmp_lt_i32_e64 s[22:23], v2, v9
	v_sub_u32_e32 v4, v2, v9
	v_add_u32_e32 v4, 0x400, v4
	v_cndmask_b32_e64 v5, 0, 1, s[34:35]
	s_and_b64 s[22:23], s[34:35], s[22:23]
	v_add_u32_e32 v2, v2, v5
	v_cndmask_b32_e64 v5, -1, v4, s[22:23]
	s_or_saveexec_b64 s[22:23], s[38:39]
	v_mov_b32_e32 v4, v3
	s_xor_b64 exec, exec, s[22:23]
	v_add_u32_e32 v4, 1, v3
	v_mov_b32_e32 v5, v3
	s_or_b64 exec, exec, s[22:23]
	v_add3_u32 v8, s70, v6, 7
	v_mov_b32_e32 v3, -1
	v_cmp_lt_i32_e64 s[22:23], -1, v5
	s_and_saveexec_b64 s[34:35], s[22:23]
	s_cbranch_execz .LBB0_2217
	v_add_u32_e32 v3, s67, v5
	v_add_u32_e32 v22, s66, v3
	v_ashrrev_i32_e32 v23, 31, v22
	v_lshlrev_b64 v[22:23], 2, v[22:23]
	v_lshl_add_u64 v[24:25], s[96:97], 0, v[22:23]
	v_lshl_add_u64 v[22:23], s[80:81], 0, v[22:23]
	v_lshrrev_b32_e32 v5, 2, v21
	global_store_dword v[22:23], v8, off
	global_store_dword v[24:25], v5, off
.LBB0_2217:
	s_or_b64 exec, exec, s[34:35]
	v_mov_b32_e32 v223, v3
	s_and_saveexec_b64 s[22:23], s[36:37]
	s_xor_b64 s[34:35], exec, s[22:23]
	v_cmp_lt_i32_e64 s[22:23], v2, v9
	v_sub_u32_e32 v3, v2, v9
	v_add_u32_e32 v3, 0x400, v3
	v_cndmask_b32_e64 v5, 0, 1, s[28:29]
	s_and_b64 s[22:23], s[28:29], s[22:23]
	v_add_u32_e32 v2, v2, v5
	v_cndmask_b32_e64 v5, -1, v3, s[22:23]
	s_or_saveexec_b64 s[22:23], s[34:35]
	v_mov_b32_e32 v3, v4
	s_xor_b64 exec, exec, s[22:23]
	v_add_u32_e32 v3, 1, v4
	v_mov_b32_e32 v5, v4
	s_or_b64 exec, exec, s[22:23]
	v_add3_u32 v8, s70, v6, 8
	v_mov_b32_e32 v4, -1
	v_cmp_lt_i32_e64 s[22:23], -1, v5
	s_and_saveexec_b64 s[28:29], s[22:23]
	s_cbranch_execz .LBB0_2223
	v_add_u32_e32 v4, s67, v5
	v_add_u32_e32 v22, s66, v4
	v_ashrrev_i32_e32 v23, 31, v22
	v_lshlrev_b64 v[22:23], 2, v[22:23]
	v_lshrrev_b32_e32 v5, 2, v20
	v_lshl_add_u64 v[20:21], s[80:81], 0, v[22:23]
	v_lshl_add_u64 v[24:25], s[96:97], 0, v[22:23]
	global_store_dword v[20:21], v8, off
	global_store_dword v[24:25], v5, off
.LBB0_2223:
	s_or_b64 exec, exec, s[28:29]
	v_mov_b32_e32 v224, v4
	s_and_saveexec_b64 s[22:23], s[30:31]
	s_xor_b64 s[28:29], exec, s[22:23]
	v_cmp_lt_i32_e64 s[22:23], v2, v9
	v_sub_u32_e32 v4, v2, v9
	v_add_u32_e32 v4, 0x400, v4
	v_cndmask_b32_e64 v5, 0, 1, s[24:25]
	s_and_b64 s[22:23], s[24:25], s[22:23]
	v_add_u32_e32 v2, v2, v5
	v_cndmask_b32_e64 v5, -1, v4, s[22:23]
	s_or_saveexec_b64 s[22:23], s[28:29]
	v_mov_b32_e32 v4, v3
	s_xor_b64 exec, exec, s[22:23]
	v_add_u32_e32 v4, 1, v3
	v_mov_b32_e32 v5, v3
	s_or_b64 exec, exec, s[22:23]
	v_add3_u32 v8, s70, v6, 9
	v_mov_b32_e32 v3, -1
	v_cmp_lt_i32_e64 s[22:23], -1, v5
	s_and_saveexec_b64 s[24:25], s[22:23]
	s_cbranch_execz .LBB0_2229
	v_add_u32_e32 v3, s67, v5
	v_add_u32_e32 v20, s66, v3
	v_ashrrev_i32_e32 v21, 31, v20
	v_lshlrev_b64 v[20:21], 2, v[20:21]
	v_lshl_add_u64 v[22:23], s[96:97], 0, v[20:21]
	v_lshl_add_u64 v[20:21], s[80:81], 0, v[20:21]
	v_lshrrev_b32_e32 v5, 2, v19
	global_store_dword v[20:21], v8, off
	global_store_dword v[22:23], v5, off
.LBB0_2229:
	s_or_b64 exec, exec, s[24:25]
	v_mov_b32_e32 v225, v3
	s_and_saveexec_b64 s[22:23], s[26:27]
	s_xor_b64 s[24:25], exec, s[22:23]
	v_cmp_lt_i32_e64 s[22:23], v2, v9
	v_sub_u32_e32 v3, v2, v9
	v_add_u32_e32 v3, 0x400, v3
	v_cndmask_b32_e64 v5, 0, 1, s[18:19]
	s_and_b64 s[18:19], s[18:19], s[22:23]
	v_add_u32_e32 v2, v2, v5
	v_cndmask_b32_e64 v5, -1, v3, s[18:19]
	s_or_saveexec_b64 s[18:19], s[24:25]
	v_mov_b32_e32 v3, v4
	s_xor_b64 exec, exec, s[18:19]
	v_add_u32_e32 v3, 1, v4
	v_mov_b32_e32 v5, v4
	s_or_b64 exec, exec, s[18:19]
	v_add3_u32 v8, s70, v6, 10
	v_mov_b32_e32 v4, -1
	v_cmp_lt_i32_e64 s[18:19], -1, v5
	s_and_saveexec_b64 s[22:23], s[18:19]
	s_cbranch_execz .LBB0_2235
	v_add_u32_e32 v4, s67, v5
	v_add_u32_e32 v20, s66, v4
	v_ashrrev_i32_e32 v21, 31, v20
	v_lshlrev_b64 v[20:21], 2, v[20:21]
	v_lshrrev_b32_e32 v5, 2, v18
	v_lshl_add_u64 v[18:19], s[80:81], 0, v[20:21]
	v_lshl_add_u64 v[22:23], s[96:97], 0, v[20:21]
	global_store_dword v[18:19], v8, off
	global_store_dword v[22:23], v5, off
.LBB0_2235:
	s_or_b64 exec, exec, s[22:23]
	v_mov_b32_e32 v226, v4
	s_and_saveexec_b64 s[18:19], s[20:21]
	s_xor_b64 s[20:21], exec, s[18:19]
	v_cmp_lt_i32_e64 s[18:19], v2, v9
	v_sub_u32_e32 v4, v2, v9
	v_add_u32_e32 v4, 0x400, v4
	v_cndmask_b32_e64 v5, 0, 1, s[14:15]
	s_and_b64 s[14:15], s[14:15], s[18:19]
	v_add_u32_e32 v2, v2, v5
	v_cndmask_b32_e64 v5, -1, v4, s[14:15]
	s_or_saveexec_b64 s[14:15], s[20:21]
	v_mov_b32_e32 v4, v3
	s_xor_b64 exec, exec, s[14:15]
	v_add_u32_e32 v4, 1, v3
	v_mov_b32_e32 v5, v3
	s_or_b64 exec, exec, s[14:15]
	v_add3_u32 v8, s70, v6, 11
	v_mov_b32_e32 v3, -1
	v_cmp_lt_i32_e64 s[14:15], -1, v5
	s_and_saveexec_b64 s[18:19], s[14:15]
	s_cbranch_execz .LBB0_2241
	v_add_u32_e32 v3, s67, v5
	v_add_u32_e32 v18, s66, v3
	v_ashrrev_i32_e32 v19, 31, v18
	v_lshlrev_b64 v[18:19], 2, v[18:19]
	v_lshl_add_u64 v[20:21], s[96:97], 0, v[18:19]
	v_lshl_add_u64 v[18:19], s[80:81], 0, v[18:19]
	v_lshrrev_b32_e32 v5, 2, v17
	global_store_dword v[18:19], v8, off
	global_store_dword v[20:21], v5, off
; template <int VPT>
; __device__ __forceinline__ void topk_list(const Params& p, LAS unsigned char* lds, const float* a, int N, int cap, int rowbase, int mbase, int e) {
;     ...
;     if (active) {
; #pragma unroll
;         for (int j = 0; j < VPT; ++j) {
;             const int i = tid * VPT + j, row = rowbase + i; int slot = -1;
;             if (k[j] > T) slot = gtb++;
;             else if (k[j] == T) { if (eqb < need) slot = G + eqb; ++eqb; }
;             if (slot >= 0) { const int m = mbase + slot; WSP(int, OFF_RIDX)[e * MEXP + m] = row; WSP(float, OFF_GATE)[e * MEXP + m] = __uint_as_float(k[j] >> 2); WSP(int, OFF_SLOT)[row * 16 + e] = m; }
;             else WSP(int, OFF_SLOT)[row * 16 + e] = -1;
;         }
;     }
.LBB0_2241:
	s_or_b64 exec, exec, s[18:19]
	v_mov_b32_e32 v227, v3
	s_and_saveexec_b64 s[14:15], s[16:17]
	s_xor_b64 s[16:17], exec, s[14:15]
	v_cmp_lt_i32_e64 s[14:15], v2, v9
	v_sub_u32_e32 v3, v2, v9
	v_add_u32_e32 v3, 0x400, v3
	v_cndmask_b32_e64 v5, 0, 1, s[10:11]
	s_and_b64 s[10:11], s[10:11], s[14:15]
	v_add_u32_e32 v2, v2, v5
	v_cndmask_b32_e64 v5, -1, v3, s[10:11]
	s_or_saveexec_b64 s[10:11], s[16:17]
	v_mov_b32_e32 v3, v4
	s_xor_b64 exec, exec, s[10:11]
	v_add_u32_e32 v3, 1, v4
	v_mov_b32_e32 v5, v4
	s_or_b64 exec, exec, s[10:11]
	v_add3_u32 v8, s70, v6, 12
	v_mov_b32_e32 v4, -1
	v_cmp_lt_i32_e64 s[10:11], -1, v5
	s_and_saveexec_b64 s[14:15], s[10:11]
	s_cbranch_execz .LBB0_2247
	v_add_u32_e32 v4, s67, v5
	v_add_u32_e32 v18, s66, v4
	v_ashrrev_i32_e32 v19, 31, v18
	v_lshlrev_b64 v[18:19], 2, v[18:19]
	v_lshrrev_b32_e32 v5, 2, v16
	v_lshl_add_u64 v[16:17], s[80:81], 0, v[18:19]
	v_lshl_add_u64 v[20:21], s[96:97], 0, v[18:19]
	global_store_dword v[16:17], v8, off
	global_store_dword v[20:21], v5, off
.LBB0_2247:
	s_or_b64 exec, exec, s[14:15]
	v_mov_b32_e32 v228, v4
	s_and_saveexec_b64 s[10:11], s[12:13]
	s_xor_b64 s[12:13], exec, s[10:11]
	v_cmp_lt_i32_e64 s[10:11], v2, v9
	v_sub_u32_e32 v4, v2, v9
	v_add_u32_e32 v4, 0x400, v4
	v_cndmask_b32_e64 v5, 0, 1, s[6:7]
	s_and_b64 s[6:7], s[6:7], s[10:11]
	v_add_u32_e32 v2, v2, v5
	v_cndmask_b32_e64 v5, -1, v4, s[6:7]
	s_or_saveexec_b64 s[6:7], s[12:13]
	v_mov_b32_e32 v4, v3
	s_xor_b64 exec, exec, s[6:7]
	v_add_u32_e32 v4, 1, v3
	v_mov_b32_e32 v5, v3
	s_or_b64 exec, exec, s[6:7]
	v_add3_u32 v8, s70, v6, 13
	v_mov_b32_e32 v3, -1
	v_cmp_lt_i32_e64 s[6:7], -1, v5
	s_and_saveexec_b64 s[10:11], s[6:7]
	s_cbranch_execz .LBB0_2253
	v_add_u32_e32 v3, s67, v5
	v_add_u32_e32 v16, s66, v3
	v_ashrrev_i32_e32 v17, 31, v16
	v_lshlrev_b64 v[16:17], 2, v[16:17]
	v_lshl_add_u64 v[18:19], s[96:97], 0, v[16:17]
	v_lshl_add_u64 v[16:17], s[80:81], 0, v[16:17]
	v_lshrrev_b32_e32 v5, 2, v15
	global_store_dword v[16:17], v8, off
	global_store_dword v[18:19], v5, off
.LBB0_2253:
	s_or_b64 exec, exec, s[10:11]
	v_mov_b32_e32 v229, v3
	s_and_saveexec_b64 s[6:7], s[8:9]
	s_xor_b64 s[8:9], exec, s[6:7]
	v_cmp_lt_i32_e64 s[6:7], v2, v9
	v_sub_u32_e32 v3, v2, v9
	v_add_u32_e32 v3, 0x400, v3
	v_cndmask_b32_e64 v5, 0, 1, s[2:3]
	s_and_b64 s[2:3], s[2:3], s[6:7]
	v_add_u32_e32 v2, v2, v5
	v_cndmask_b32_e64 v8, -1, v3, s[2:3]
	s_or_saveexec_b64 s[2:3], s[8:9]
	v_mov_b32_e32 v5, v4
	s_xor_b64 exec, exec, s[2:3]
	v_add_u32_e32 v5, 1, v4
	v_mov_b32_e32 v8, v4
	s_or_b64 exec, exec, s[2:3]
	v_add3_u32 v15, s70, v6, 14
	v_mov_b32_e32 v3, -1
	v_cmp_lt_i32_e64 s[2:3], -1, v8
	v_mov_b32_e32 v4, -1
	s_and_saveexec_b64 s[6:7], s[2:3]
	s_cbranch_execz .LBB0_2259
	v_add_u32_e32 v4, s67, v8
	v_add_u32_e32 v16, s66, v4
	v_ashrrev_i32_e32 v17, 31, v16
	v_lshlrev_b64 v[16:17], 2, v[16:17]
	v_lshl_add_u64 v[18:19], s[96:97], 0, v[16:17]
	v_lshl_add_u64 v[16:17], s[80:81], 0, v[16:17]
	v_lshrrev_b32_e32 v8, 2, v14
	global_store_dword v[16:17], v15, off
	global_store_dword v[18:19], v8, off
.LBB0_2259:
	s_or_b64 exec, exec, s[6:7]
	v_cmp_lt_i32_e64 s[2:3], v2, v9
	v_sub_u32_e32 v2, v2, v9
	v_add_u32_e32 v2, 0x400, v2
	s_and_b64 s[0:1], s[0:1], s[2:3]
	v_cndmask_b32_e64 v2, -1, v2, s[0:1]
	v_cndmask_b32_e32 v2, v2, v5, vcc
	v_mov_b32_e32 v230, v4
	v_add3_u32 v4, s70, v6, 15
	v_cmp_lt_i32_e32 vcc, -1, v2
	s_and_saveexec_b64 s[0:1], vcc
	s_cbranch_execz .LBB0_2261
	v_add_u32_e32 v3, s67, v2
	v_add_u32_e32 v8, s66, v3
	v_ashrrev_i32_e32 v9, 31, v8
	v_lshlrev_b64 v[8:9], 2, v[8:9]
	v_lshrrev_b32_e32 v2, 2, v7
	v_lshl_add_u64 v[6:7], s[80:81], 0, v[8:9]
	v_lshl_add_u64 v[14:15], s[96:97], 0, v[8:9]
	global_store_dword v[6:7], v4, off
	global_store_dword v[14:15], v2, off
.LBB0_2261:
	s_or_b64 exec, exec, s[0:1]
	v_mov_b32_e32 v231, v3
	s_mul_i32 s98, s92, 0x4200
	v_subrev_u32_e32 v4, 15, v4
	v_add_u32_e32 v4, s98, v4
	v_ashrrev_i32_e32 v5, 31, v4
	v_lshl_add_u64 v[4:5], v[4:5], 2, s[4:5]
	global_store_dwordx4 v[4:5], v[216:219], off
	global_store_dwordx4 v[4:5], v[220:223], off offset:16
	global_store_dwordx4 v[4:5], v[224:227], off offset:32
	global_store_dwordx4 v[4:5], v[228:231], off offset:48
